# speedup vs baseline: 1.0282x; 1.0060x over previous
_Z7xform_xPKfP15HIP_vector_typeIjLj4EE:
	s_load_dwordx4 s[4:7], s[0:1], 0x0
	s_lshr_b32 s8, s2, 2
	s_and_b32 s9, s2, 3
	v_and_b32_e32 v1, 15, v0
	v_lshrrev_b32_e32 v2, 4, v0
	v_lshrrev_b32_e32 v3, 3, v2
	v_and_b32_e32 v4, 7, v2
	s_lshl_b32 s10, s9, 3
	v_add_u32_e32 v5, s10, v4
	v_lshlrev_b32_e32 v5, 14, v5
	v_lshl_add_u32 v5, v3, 19, v5
	v_lshl_add_u32 v5, v1, 4, v5
	s_lshl_b32 s11, s8, 8
	v_add_u32_e32 v5, s11, v5
	v_xor_b32_e32 v40, v1, v3
	v_lshlrev_b32_e32 v42, 8, v2
	s_waitcnt lgkmcnt(0)
	s_mov_b32 s12, s4
	s_and_b32 s13, s5, 0xffff
	s_mov_b32 s14, 0x800000
	s_mov_b32 s15, 0x20000
	s_mov_b32 s16, s6
	s_and_b32 s17, s7, 0xffff
	s_mov_b32 s18, 0x400000
	s_mov_b32 s19, 0x20000
	s_mov_b32 s20, 0x0
	s_mov_b32 s21, 0x100000
	s_mov_b32 s22, 0x200000
	s_mov_b32 s23, 0x300000
	s_mov_b32 s24, 0x400000
	s_mov_b32 s25, 0x500000
	s_mov_b32 s26, 0x600000
	s_mov_b32 s27, 0x700000
	buffer_load_dwordx4 v[8:11], v5, s[12:15], s20 offen nt
	buffer_load_dwordx4 v[12:15], v5, s[12:15], s21 offen nt
	buffer_load_dwordx4 v[16:19], v5, s[12:15], s22 offen nt
	buffer_load_dwordx4 v[20:23], v5, s[12:15], s23 offen nt
	buffer_load_dwordx4 v[24:27], v5, s[12:15], s24 offen nt
	buffer_load_dwordx4 v[28:31], v5, s[12:15], s25 offen nt
	buffer_load_dwordx4 v[32:35], v5, s[12:15], s26 offen nt
	buffer_load_dwordx4 v[36:39], v5, s[12:15], s27 offen nt
	v_lshrrev_b32_e32 v43, 6, v0
	v_bfe_u32 v44, v0, 4, 2
	v_and_b32_e32 v45, 3, v1
	v_xor_b32_e32 v45, v43, v45
	v_lshlrev_b32_e32 v45, 4, v45
	v_lshl_add_u32 v45, v1, 11, v45
	v_lshl_add_u32 v45, v44, 2, v45
	v_lshrrev_b32_e32 v46, 2, v1
	s_lshl_b32 s28, s8, 16
	s_lshl_b32 s29, s9, 8
	s_add_u32 s28, s28, s29
	v_lshlrev_b32_e32 v48, 10, v2
	v_lshl_add_u32 v48, v1, 4, v48
	v_add_u32_e32 v48, s28, v48
	s_waitcnt vmcnt(7)
	v_xor_b32_e32 v41, 0, v40
	v_lshl_add_u32 v41, v41, 4, v42
	ds_write_b128 v41, v[8:11] offset:0
	s_waitcnt vmcnt(6)
	v_xor_b32_e32 v41, 2, v40
	v_lshl_add_u32 v41, v41, 4, v42
	ds_write_b128 v41, v[12:15] offset:4096
	s_waitcnt vmcnt(5)
	v_xor_b32_e32 v41, 4, v40
	v_lshl_add_u32 v41, v41, 4, v42
	ds_write_b128 v41, v[16:19] offset:8192
	s_waitcnt vmcnt(4)
	v_xor_b32_e32 v41, 6, v40
	v_lshl_add_u32 v41, v41, 4, v42
	ds_write_b128 v41, v[20:23] offset:12288
	s_waitcnt vmcnt(3)
	v_xor_b32_e32 v41, 8, v40
	v_lshl_add_u32 v41, v41, 4, v42
	ds_write_b128 v41, v[24:27] offset:16384
	s_waitcnt vmcnt(2)
	v_xor_b32_e32 v41, 10, v40
	v_lshl_add_u32 v41, v41, 4, v42
	ds_write_b128 v41, v[28:31] offset:20480
	s_waitcnt vmcnt(1)
	v_xor_b32_e32 v41, 12, v40
	v_lshl_add_u32 v41, v41, 4, v42
	ds_write_b128 v41, v[32:35] offset:24576
	s_waitcnt vmcnt(0)
	v_xor_b32_e32 v41, 14, v40
	v_lshl_add_u32 v41, v41, 4, v42
	ds_write_b128 v41, v[36:39] offset:28672
	s_waitcnt lgkmcnt(0)
	s_barrier
	v_xor_b32_e32 v47, 0, v46
	v_lshl_add_u32 v47, v47, 6, v45
	v_xor_b32_e32 v49, 1, v46
	v_lshl_add_u32 v49, v49, 6, v45
	ds_read2st64_b32 v[50:51], v47 offset0:0 offset1:1
	ds_read2st64_b32 v[52:53], v47 offset0:2 offset1:3
	ds_read2st64_b32 v[54:55], v47 offset0:4 offset1:5
	ds_read2st64_b32 v[56:57], v47 offset0:6 offset1:7
	ds_read2st64_b32 v[58:59], v49 offset0:0 offset1:1
	ds_read2st64_b32 v[60:61], v49 offset0:2 offset1:3
	ds_read2st64_b32 v[62:63], v49 offset0:4 offset1:5
	ds_read2st64_b32 v[64:65], v49 offset0:6 offset1:7
	s_waitcnt lgkmcnt(7)
	v_cvt_pk_f16_f32 v8, v50, v51
	s_waitcnt lgkmcnt(6)
	v_cvt_pk_f16_f32 v9, v52, v53
	s_waitcnt lgkmcnt(5)
	v_cvt_pk_f16_f32 v10, v54, v55
	s_waitcnt lgkmcnt(4)
	v_cvt_pk_f16_f32 v11, v56, v57
	s_mov_b32 s30, 0x0
	buffer_store_dwordx4 v[8:11], v48, s[16:19], s30 offen
	s_waitcnt lgkmcnt(3)
	v_cvt_pk_f16_f32 v12, v58, v59
	s_waitcnt lgkmcnt(2)
	v_cvt_pk_f16_f32 v13, v60, v61
	s_waitcnt lgkmcnt(1)
	v_cvt_pk_f16_f32 v14, v62, v63
	s_waitcnt lgkmcnt(0)
	v_cvt_pk_f16_f32 v15, v64, v65
	s_mov_b32 s30, 0x4000
	buffer_store_dwordx4 v[12:15], v48, s[16:19], s30 offen
	v_xor_b32_e32 v47, 2, v46
	v_lshl_add_u32 v47, v47, 6, v45
	v_xor_b32_e32 v49, 3, v46
	v_lshl_add_u32 v49, v49, 6, v45
	ds_read2st64_b32 v[50:51], v47 offset0:0 offset1:1
	ds_read2st64_b32 v[52:53], v47 offset0:2 offset1:3
	ds_read2st64_b32 v[54:55], v47 offset0:4 offset1:5
	ds_read2st64_b32 v[56:57], v47 offset0:6 offset1:7
	ds_read2st64_b32 v[58:59], v49 offset0:0 offset1:1
	ds_read2st64_b32 v[60:61], v49 offset0:2 offset1:3
	ds_read2st64_b32 v[62:63], v49 offset0:4 offset1:5
	ds_read2st64_b32 v[64:65], v49 offset0:6 offset1:7
	s_waitcnt lgkmcnt(7)
	v_cvt_pk_f16_f32 v16, v50, v51
	s_waitcnt lgkmcnt(6)
	v_cvt_pk_f16_f32 v17, v52, v53
	s_waitcnt lgkmcnt(5)
	v_cvt_pk_f16_f32 v18, v54, v55
	s_waitcnt lgkmcnt(4)
	v_cvt_pk_f16_f32 v19, v56, v57
	s_mov_b32 s30, 0x8000
	buffer_store_dwordx4 v[16:19], v48, s[16:19], s30 offen
	s_waitcnt lgkmcnt(3)
	v_cvt_pk_f16_f32 v20, v58, v59
	s_waitcnt lgkmcnt(2)
	v_cvt_pk_f16_f32 v21, v60, v61
	s_waitcnt lgkmcnt(1)
	v_cvt_pk_f16_f32 v22, v62, v63
	s_waitcnt lgkmcnt(0)
	v_cvt_pk_f16_f32 v23, v64, v65
	s_mov_b32 s30, 0xc000
	buffer_store_dwordx4 v[20:23], v48, s[16:19], s30 offen
	s_endpgm
